# speedup vs baseline: 1.0189x; 1.0189x over previous
.LBB0_34:
	s_andn2_b64 vcc, exec, s[6:7]
	s_cbranch_vccnz .LBB0_41
	s_load_dwordx2 s[10:11], s[0:1], 0x28
	s_movk_i32 s3, 0x300
	v_cmp_gt_u32_e32 vcc, s3, v0
	s_and_saveexec_b64 s[6:7], vcc
	s_cbranch_execz .LBB0_38
	v_lshlrev_b32_e32 v2, 6, v0
	v_mov_b32_e32 v3, 0
	s_waitcnt lgkmcnt(0)
	v_lshl_add_u64 v[4:5], s[8:9], 0, v[2:3]
	s_mov_b64 s[12:13], 0x140000
	v_or_b32_e32 v1, 0xffffff00, v0
	v_lshl_add_u64 v[4:5], v[4:5], 0, s[12:13]
	s_mov_b64 s[12:13], 0
	v_mov_b32_e32 v2, v3
	s_mov_b64 s[14:15], 0x4000
	s_movk_i32 s3, 0x1ff

.LBB5_99:
	s_or_b64 exec, exec, s[18:19]
	s_waitcnt lgkmcnt(0)
	s_barrier
	v_or_b32_e32 v1, s45, v128
	v_cmp_eq_u32_e64 s[8:9], 0, v1
	s_and_saveexec_b64 s[16:17], s[8:9]
	s_cbranch_execz .LBB5_101
	v_mov_b32_e32 v61, 0x23e40
	ds_read_b128 v[42:45], v61
	ds_read_b128 v[46:49], v61 offset:16
	ds_read_b128 v[50:53], v61 offset:32
	ds_read_b128 v[54:57], v61 offset:48
	ds_read_b128 v[58:61], v61 offset:64
	s_lshl_b32 s18, s33, 11
	s_add_u32 s28, s34, s18
	s_addc_u32 s29, s35, 0
	s_ashr_i32 s37, s36, 31
	s_lshl_b64 s[18:19], s[36:37], 6
	s_add_u32 s18, s28, s18
	s_addc_u32 s19, s29, s19
	s_waitcnt lgkmcnt(4)
	v_add_f32_e32 v42, 0, v42
	v_add_f32_e32 v43, 0, v43
	v_add_f32_e32 v42, v42, v44
	v_add_f32_e32 v43, v43, v45
	s_waitcnt lgkmcnt(3)
	v_add_f32_e32 v42, v42, v46
	v_add_f32_e32 v43, v43, v47
	v_add_f32_e32 v42, v42, v48
	v_add_f32_e32 v43, v43, v49
	s_waitcnt lgkmcnt(2)
	v_add_f32_e32 v42, v42, v50
	v_add_f32_e32 v43, v43, v51
	v_add_f32_e32 v42, v42, v52
	v_add_f32_e32 v43, v43, v53
	s_waitcnt lgkmcnt(1)
	v_add_f32_e32 v42, v42, v54
	v_add_f32_e32 v43, v43, v55
	v_add_f32_e32 v42, v42, v56
	v_add_f32_e32 v43, v43, v57
	s_waitcnt lgkmcnt(0)
	v_add_f32_e32 v42, v42, v58
	v_add_f32_e32 v43, v43, v59
	v_add_f32_e32 v42, v42, v60
	v_add_f32_e32 v43, v43, v61
	v_or_b32_e32 v43, 1, v43
	v_mov_b32_e32 v61, 0x140000
	global_store_dwordx2 v61, v[42:43], s[18:19] sc1

.LBB5_107:
	s_cmp_lt_u32 s47, 64
	s_cselect_b64 s[16:17], -1, 0
	s_cmp_gt_u32 s47, 63
	v_cmp_gt_u32_e64 s[10:11], 31, v128
	v_cmp_lt_u32_e64 s[12:13], 30, v128
	v_lshlrev_b32_e32 v82, 6, v128
	s_cbranch_scc1 .LBB5_130
	s_lshl_b32 s18, s33, 11
	s_add_u32 s18, s34, s18
	s_addc_u32 s19, s35, 0
	v_mov_b32_e32 v83, 0
	v_lshl_add_u64 v[2:3], s[18:19], 0, v[82:83]
	s_mov_b64 s[18:19], 0x140000
	v_lshl_add_u64 v[2:3], v[2:3], 0, s[18:19]
	v_mov_b64_e32 v[4:5], 0
	s_mov_b32 s30, 0x400001
	s_mov_b64 s[18:19], 0xffffffff
	s_branch .LBB5_110

.LBB5_141:
	s_or_b64 exec, exec, s[24:25]
	s_waitcnt lgkmcnt(0)
	s_barrier
	s_and_saveexec_b64 s[12:13], s[8:9]
	s_cbranch_execz .LBB5_143
	v_mov_b32_e32 v73, 0x23e40
	ds_read_b128 v[54:57], v73
	ds_read_b128 v[58:61], v73 offset:16
	ds_read_b128 v[62:65], v73 offset:32
	ds_read_b128 v[66:69], v73 offset:48
	ds_read_b128 v[70:73], v73 offset:64
	s_lshl_b32 s18, s33, 11
	s_add_u32 s24, s34, s18
	s_addc_u32 s25, s35, 0
	s_ashr_i32 s37, s36, 31
	s_lshl_b64 s[18:19], s[36:37], 6
	s_add_u32 s18, s24, s18
	s_addc_u32 s19, s25, s19
	s_waitcnt lgkmcnt(4)
	v_add_f32_e32 v54, 0, v54
	v_add_f32_e32 v55, 0, v55
	v_add_f32_e32 v54, v54, v56
	v_add_f32_e32 v55, v55, v57
	s_waitcnt lgkmcnt(3)
	v_add_f32_e32 v54, v54, v58
	v_add_f32_e32 v55, v55, v59
	v_add_f32_e32 v54, v54, v60
	v_add_f32_e32 v55, v55, v61
	s_waitcnt lgkmcnt(2)
	v_add_f32_e32 v54, v54, v62
	v_add_f32_e32 v55, v55, v63
	v_add_f32_e32 v54, v54, v64
	v_add_f32_e32 v55, v55, v65
	s_waitcnt lgkmcnt(1)
	v_add_f32_e32 v54, v54, v66
	v_add_f32_e32 v55, v55, v67
	v_add_f32_e32 v54, v54, v68
	v_add_f32_e32 v55, v55, v69
	s_waitcnt lgkmcnt(0)
	v_add_f32_e32 v54, v54, v70
	v_add_f32_e32 v55, v55, v71
	v_add_f32_e32 v54, v54, v72
	v_add_f32_e32 v55, v55, v73
	v_or_b32_e32 v55, 1, v55
	v_mov_b32_e32 v73, 0x144000
	global_store_dwordx2 v73, v[54:55], s[18:19] sc1

.LBB5_150:
	s_lshl_b32 s10, s33, 11
	s_add_u32 s16, s34, s10
	s_addc_u32 s17, s35, 0
	v_mov_b32_e32 v83, 0
	v_lshl_add_u64 v[0:1], s[16:17], 0, v[82:83]
	s_mov_b64 s[16:17], 0x144000
	v_cmp_gt_u32_e64 s[10:11], 31, v128
	v_cmp_lt_u32_e64 s[12:13], 30, v128
	v_lshl_add_u64 v[0:1], v[0:1], 0, s[16:17]
	v_mov_b64_e32 v[2:3], 0
	s_mov_b32 s24, 0x400001
	s_mov_b64 s[16:17], 0xffffffff
	s_sleep 16
	s_branch .LBB5_152

.LBB5_177:
	s_or_b64 exec, exec, s[14:15]
	s_waitcnt lgkmcnt(0)
	s_barrier
	s_and_saveexec_b64 s[10:11], s[8:9]
	s_cbranch_execz .LBB5_179
	v_mov_b32_e32 v43, 0x23e40
	ds_read_b128 v[24:27], v43
	ds_read_b128 v[28:31], v43 offset:16
	ds_read_b128 v[32:35], v43 offset:32
	ds_read_b128 v[36:39], v43 offset:48
	ds_read_b128 v[40:43], v43 offset:64
	s_waitcnt vmcnt(8)
	s_lshl_b32 s8, s33, 11
	s_add_u32 s12, s34, s8
	s_addc_u32 s13, s35, 0
	s_ashr_i32 s37, s36, 31
	s_lshl_b64 s[8:9], s[36:37], 6
	s_add_u32 s8, s12, s8
	s_addc_u32 s9, s13, s9
	s_waitcnt lgkmcnt(4)
	v_add_f32_e32 v24, 0, v24
	v_add_f32_e32 v25, 0, v25
	v_add_f32_e32 v24, v24, v26
	v_add_f32_e32 v25, v25, v27
	s_waitcnt lgkmcnt(3)
	v_add_f32_e32 v24, v24, v28
	v_add_f32_e32 v25, v25, v29
	v_add_f32_e32 v24, v24, v30
	v_add_f32_e32 v25, v25, v31
	s_waitcnt lgkmcnt(2)
	v_add_f32_e32 v24, v24, v32
	v_add_f32_e32 v25, v25, v33
	v_add_f32_e32 v24, v24, v34
	v_add_f32_e32 v25, v25, v35
	s_waitcnt lgkmcnt(1)
	v_add_f32_e32 v24, v24, v36
	v_add_f32_e32 v25, v25, v37
	v_add_f32_e32 v24, v24, v38
	v_add_f32_e32 v25, v25, v39
	s_waitcnt lgkmcnt(0)
	v_add_f32_e32 v24, v24, v40
	v_add_f32_e32 v25, v25, v41
	v_add_f32_e32 v24, v24, v42
	v_add_f32_e32 v25, v25, v43
	v_or_b32_e32 v25, 1, v25
	v_mov_b32_e32 v43, 0x148000
	global_store_dwordx2 v43, v[24:25], s[8:9] sc1

.LBB5_184:
	s_lshl_b32 s2, s33, 11
	s_add_u32 s8, s34, s2
	s_addc_u32 s9, s35, 0
	v_mov_b32_e32 v83, 0
	s_waitcnt vmcnt(7)
	v_lshl_add_u64 v[36:37], s[8:9], 0, v[82:83]
	s_mov_b64 s[8:9], 0x148000
	v_cmp_gt_u32_e64 s[2:3], 31, v128
	v_cmp_lt_u32_e64 s[4:5], 30, v128
	v_lshl_add_u64 v[36:37], v[36:37], 0, s[8:9]
	s_waitcnt vmcnt(6)
	v_mov_b64_e32 v[38:39], 0
	s_mov_b32 s12, 0x400001
	s_mov_b64 s[8:9], 0xffffffff
	s_sleep 16
	s_branch .LBB5_186
